# baseline (speedup 1.0000x reference)
	.amdhsa_kernel _Z16bilateral_kernelPKfS0_Pf
		.amdhsa_group_segment_fixed_size 0
		.amdhsa_private_segment_fixed_size 0
		.amdhsa_kernarg_size 24
		.amdhsa_user_sgpr_count 2
		.amdhsa_user_sgpr_dispatch_ptr 0
		.amdhsa_user_sgpr_queue_ptr 0
		.amdhsa_user_sgpr_kernarg_segment_ptr 1
		.amdhsa_user_sgpr_dispatch_id 0
		.amdhsa_user_sgpr_kernarg_preload_length 0
		.amdhsa_user_sgpr_kernarg_preload_offset 0
		.amdhsa_user_sgpr_private_segment_size 0
		.amdhsa_uses_dynamic_stack 0
		.amdhsa_enable_private_segment 0
		.amdhsa_system_sgpr_workgroup_id_x 1
		.amdhsa_system_sgpr_workgroup_id_y 0
		.amdhsa_system_sgpr_workgroup_id_z 0
		.amdhsa_system_sgpr_workgroup_info 0
		.amdhsa_system_vgpr_workitem_id 0
		.amdhsa_next_free_vgpr 120
		.amdhsa_next_free_sgpr 40
		.amdhsa_accum_offset 120
		.amdhsa_reserve_vcc 1
		.amdhsa_float_round_mode_32 0
		.amdhsa_float_round_mode_16_64 0
		.amdhsa_float_denorm_mode_32 3
		.amdhsa_float_denorm_mode_16_64 3
		.amdhsa_dx10_clamp 1
		.amdhsa_ieee_mode 1
		.amdhsa_fp16_overflow 0
		.amdhsa_tg_split 0
		.amdhsa_exception_fp_ieee_invalid_op 0
		.amdhsa_exception_fp_denorm_src 0
		.amdhsa_exception_fp_ieee_div_zero 0
		.amdhsa_exception_fp_ieee_overflow 0
		.amdhsa_exception_fp_ieee_underflow 0
		.amdhsa_exception_fp_ieee_inexact 0
		.amdhsa_exception_int_div_zero 0
	.end_amdhsa_kernel

amdhsa.kernels:
  - .agpr_count:     0
    .args:
      - .actual_access:  read_only
        .address_space:  global
        .offset:         0
        .size:           8
        .value_kind:     global_buffer
      - .actual_access:  read_only
        .address_space:  global
        .offset:         8
        .size:           8
        .value_kind:     global_buffer
      - .actual_access:  write_only
        .address_space:  global
        .offset:         16
        .size:           8
        .value_kind:     global_buffer
    .group_segment_fixed_size: 0
    .kernarg_segment_align: 8
    .kernarg_segment_size: 24
    .language:       OpenCL C
    .language_version:
      - 2
      - 0
    .max_flat_workgroup_size: 256
    .name:           _Z16bilateral_kernelPKfS0_Pf
    .private_segment_fixed_size: 0
    .sgpr_count:     46
    .sgpr_spill_count: 0
    .symbol:         _Z16bilateral_kernelPKfS0_Pf.kd
    .uniform_work_group_size: 1
    .uses_dynamic_stack: false
    .vgpr_count:     120
    .vgpr_spill_count: 0
    .wavefront_size: 64
